# stick-breaking attention LDS sweep: next tile K fragments prefetched during the current tile VALU section, on top of v41
# baseline (speedup 1.0000x reference)
.LBB0_301:
	s_ashr_i32 s2, s72, 9
	s_lshl_b32 s3, s72, 8
	s_and_b32 s75, s3, 0x1f00
	s_ashr_i32 s3, s2, 31
	v_readlane_b32 s4, v239, 14
	s_bfe_u32 s43, s72, 0x40005
	s_lshl_b64 s[46:47], s[2:3], 13
	s_add_i32 s42, s75, s4
	s_mov_b64 s[40:41], s[78:79]
	v_mov_b32_e32 v34, v0
	s_add_u32 s4, s46, s42
	s_addc_u32 s5, s47, 0
	v_and_b32_e32 v19, 31, v34
	v_or_b32_e32 v82, s4, v19
	v_mov_b32_e32 v83, s5
	v_lshlrev_b64 v[2:3], 12, v[82:83]
	v_lshrrev_b32_e32 v5, 1, v34
	v_lshl_add_u64 v[2:3], s[0:1], 0, v[2:3]
	s_lshl_b32 s84, s43, 7
	v_lshl_add_u64 v[2:3], v[2:3], 0, s[84:85]
	v_and_b32_e32 v166, 16, v5
	v_add_u32_e32 v80, 0x600, v34
	v_lshl_add_u64 v[2:3], v[2:3], 0, v[166:167]
	s_addk_i32 s75, 0xff00
	v_ashrrev_i32_e32 v35, 3, v34
	v_ashrrev_i32_e32 v81, 3, v80
	global_load_dwordx4 v[50:53], v[2:3], off
	global_load_dwordx4 v[54:57], v[2:3], off offset:32
	global_load_dwordx4 v[58:61], v[2:3], off offset:64
	global_load_dwordx4 v[62:65], v[2:3], off offset:96
	v_add_u32_e32 v2, s75, v35
	v_add_u32_e32 v16, s75, v81
	v_max_i32_e32 v2, 0, v2
	v_mov_b32_e32 v3, v167
	v_max_i32_e32 v16, 0, v16
	v_mov_b32_e32 v17, v167
	v_lshl_add_u64 v[2:3], s[46:47], 0, v[2:3]
	v_lshl_add_u64 v[16:17], s[46:47], 0, v[16:17]
	v_lshlrev_b64 v[2:3], 12, v[2:3]
	v_lshlrev_b64 v[16:17], 12, v[16:17]
	v_lshlrev_b32_e32 v4, 2, v34
	v_lshl_add_u64 v[2:3], s[0:1], 0, v[2:3]
	v_lshlrev_b32_e32 v48, 4, v34
	v_lshl_add_u64 v[16:17], s[0:1], 0, v[16:17]
	v_and_b32_e32 v68, 12, v5
	v_and_b32_e32 v70, 16, v4
	v_lshl_add_u64 v[4:5], v[2:3], 0, s[84:85]
	v_and_b32_e32 v2, 0x70, v48
	v_mov_b32_e32 v3, v167
	v_lshl_add_u64 v[16:17], v[16:17], 0, s[84:85]
	s_waitcnt vmcnt(35)
	v_add_u32_e32 v88, 0x800, v34
	v_lshl_add_u64 v[16:17], v[16:17], 0, v[2:3]
	s_waitcnt vmcnt(19)
	v_ashrrev_i32_e32 v104, 3, v88
	global_load_dwordx4 v[20:23], v[16:17], off offset:2048
	v_add_u32_e32 v16, s75, v104
	v_max_i32_e32 v16, 0, v16
	v_mov_b32_e32 v17, v167
	v_lshl_add_u64 v[16:17], s[46:47], 0, v[16:17]
	v_lshlrev_b64 v[16:17], 12, v[16:17]
	v_lshl_add_u64 v[16:17], s[0:1], 0, v[16:17]
	v_lshl_add_u64 v[16:17], v[16:17], 0, s[84:85]
	v_add_u32_e32 v92, 0xa00, v34
	v_lshl_add_u64 v[16:17], v[16:17], 0, v[2:3]
	v_ashrrev_i32_e32 v105, 3, v92
	global_load_dwordx4 v[24:27], v[16:17], off offset:2048
	v_add_u32_e32 v16, s75, v105
	v_max_i32_e32 v16, 0, v16
	v_mov_b32_e32 v17, v167
	v_lshl_add_u64 v[16:17], s[46:47], 0, v[16:17]
	v_lshlrev_b64 v[16:17], 12, v[16:17]
	v_lshl_add_u64 v[16:17], s[0:1], 0, v[16:17]
	v_add_u32_e32 v49, 0x200, v34
	v_lshl_add_u64 v[16:17], v[16:17], 0, s[84:85]
	v_add_u32_e32 v96, 0xc00, v34
	v_ashrrev_i32_e32 v66, 3, v49
	v_lshl_add_u64 v[16:17], v[16:17], 0, v[2:3]
	v_ashrrev_i32_e32 v106, 3, v96
	v_add_u32_e32 v8, s75, v66
	global_load_dwordx4 v[28:31], v[16:17], off offset:2048
	v_add_u32_e32 v16, s75, v106
	v_max_i32_e32 v8, 0, v8
	v_mov_b32_e32 v9, v167
	v_add_u32_e32 v67, 0x400, v34
	v_max_i32_e32 v16, 0, v16
	v_mov_b32_e32 v17, v167
	v_lshl_add_u64 v[8:9], s[46:47], 0, v[8:9]
	v_ashrrev_i32_e32 v71, 3, v67
	v_lshl_add_u64 v[16:17], s[46:47], 0, v[16:17]
	v_lshl_add_u64 v[4:5], v[4:5], 0, v[2:3]
	v_lshlrev_b64 v[8:9], 12, v[8:9]
	v_add_u32_e32 v12, s75, v71
	v_lshlrev_b64 v[16:17], 12, v[16:17]
	global_load_dwordx4 v[4:7], v[4:5], off offset:2048
	v_lshl_add_u64 v[8:9], s[0:1], 0, v[8:9]
	v_max_i32_e32 v12, 0, v12
	v_mov_b32_e32 v13, v167
	v_lshl_add_u64 v[16:17], s[0:1], 0, v[16:17]
	v_lshl_add_u64 v[8:9], v[8:9], 0, s[84:85]
	v_lshl_add_u64 v[12:13], s[46:47], 0, v[12:13]
	v_lshl_add_u64 v[16:17], v[16:17], 0, s[84:85]
	v_add_u32_e32 v100, 0xe00, v34
	v_lshl_add_u64 v[8:9], v[8:9], 0, v[2:3]
	v_lshlrev_b64 v[12:13], 12, v[12:13]
	v_lshl_add_u64 v[16:17], v[16:17], 0, v[2:3]
	v_ashrrev_i32_e32 v107, 3, v100
	global_load_dwordx4 v[8:11], v[8:9], off offset:2048
	v_lshl_add_u64 v[12:13], s[0:1], 0, v[12:13]
	global_load_dwordx4 v[36:39], v[16:17], off offset:2048
	v_add_u32_e32 v16, s75, v107
	v_lshl_add_u64 v[12:13], v[12:13], 0, s[84:85]
	v_max_i32_e32 v16, 0, v16
	v_mov_b32_e32 v17, v167
	v_lshl_add_u64 v[12:13], v[12:13], 0, v[2:3]
	v_lshl_add_u64 v[16:17], s[46:47], 0, v[16:17]
	global_load_dwordx4 v[12:15], v[12:13], off offset:2048
	v_lshlrev_b64 v[16:17], 12, v[16:17]
	v_lshl_add_u64 v[16:17], s[0:1], 0, v[16:17]
	v_lshlrev_b32_e32 v32, 3, v34
	v_lshl_add_u64 v[16:17], v[16:17], 0, s[84:85]
	v_lshl_add_u64 v[16:17], v[16:17], 0, v[2:3]
	v_and_b32_e32 v3, 0x1f8, v32
	v_add_u32_e32 v3, s75, v3
	v_max_i32_e32 v3, 0, v3
	s_lshl_b32 s74, s43, 6
	global_load_dwordx4 v[40:43], v[16:17], off offset:2048
	s_lshl_b64 s[48:49], s[2:3], 14
	v_lshlrev_b32_e32 v16, 1, v3
	v_ashrrev_i32_e32 v3, 6, v34
	s_add_u32 s2, s67, s48
	v_add_u32_e32 v32, s74, v3
	s_addc_u32 s3, s68, s49
	v_mov_b32_e32 v17, v167
	v_ashrrev_i32_e32 v33, 31, v32
	v_lshl_add_u64 v[16:17], s[2:3], 0, v[16:17]
	v_lshlrev_b64 v[32:33], 15, v[32:33]
	v_lshl_add_u64 v[32:33], v[16:17], 0, v[32:33]
	v_ashrrev_i32_e32 v49, 6, v49
	global_load_dwordx4 v[44:47], v[32:33], off
	v_add_u32_e32 v32, s74, v49
	v_ashrrev_i32_e32 v33, 31, v32
	v_lshlrev_b64 v[32:33], 15, v[32:33]
	v_lshl_add_u64 v[32:33], v[16:17], 0, v[32:33]
	v_ashrrev_i32_e32 v67, 6, v67
	global_load_dwordx4 v[72:75], v[32:33], off
	v_add_u32_e32 v32, s74, v67
	v_ashrrev_i32_e32 v33, 31, v32
	v_lshlrev_b64 v[32:33], 15, v[32:33]
	v_lshl_add_u64 v[32:33], v[16:17], 0, v[32:33]
	v_ashrrev_i32_e32 v80, 6, v80
	global_load_dwordx4 v[76:79], v[32:33], off
	v_add_u32_e32 v32, s74, v80
	v_ashrrev_i32_e32 v33, 31, v32
	v_lshlrev_b64 v[32:33], 15, v[32:33]
	v_lshl_add_u64 v[32:33], v[16:17], 0, v[32:33]
	v_ashrrev_i32_e32 v108, 6, v88
	global_load_dwordx4 v[84:87], v[32:33], off
	v_add_u32_e32 v32, s74, v108
	v_ashrrev_i32_e32 v33, 31, v32
	v_lshlrev_b64 v[32:33], 15, v[32:33]
	v_lshl_add_u64 v[32:33], v[16:17], 0, v[32:33]
	v_ashrrev_i32_e32 v109, 6, v92
	global_load_dwordx4 v[88:91], v[32:33], off
	v_add_u32_e32 v32, s74, v109
	v_ashrrev_i32_e32 v33, 31, v32
	v_lshlrev_b64 v[32:33], 15, v[32:33]
	v_lshl_add_u64 v[32:33], v[16:17], 0, v[32:33]
	v_ashrrev_i32_e32 v110, 6, v96
	global_load_dwordx4 v[92:95], v[32:33], off
	v_add_u32_e32 v32, s74, v110
	v_ashrrev_i32_e32 v33, 31, v32
	v_lshlrev_b64 v[32:33], 15, v[32:33]
	v_lshl_add_u64 v[32:33], v[16:17], 0, v[32:33]
	global_load_dwordx4 v[96:99], v[32:33], off
	v_ashrrev_i32_e32 v111, 6, v100
	v_add_u32_e32 v32, s74, v111
	v_ashrrev_i32_e32 v33, 31, v32
	v_lshlrev_b64 v[32:33], 15, v[32:33]
	v_lshl_add_u64 v[16:17], v[16:17], 0, v[32:33]
	global_load_dwordx4 v[100:103], v[16:17], off
	s_movk_i32 s15, 0x90
	v_mul_lo_u32 v16, v35, s15
	v_add_u32_e32 v16, 0, v16
	v_and_b32_e32 v17, 16, v35
	v_add3_u32 v16, v16, v17, v2
	s_barrier
	s_waitcnt vmcnt(12)
	ds_write_b128 v16, v[4:7]
	v_mul_lo_u32 v4, v66, s15
	v_add_u32_e32 v4, 0, v4
	v_and_b32_e32 v5, 16, v66
	v_add3_u32 v4, v4, v5, v2
	s_waitcnt vmcnt(11)
	ds_write_b128 v4, v[8:11]
	v_mul_lo_u32 v4, v71, s15
	v_add_u32_e32 v4, 0, v4
	v_and_b32_e32 v5, 16, v71
	v_add3_u32 v4, v4, v5, v2
	s_waitcnt vmcnt(9)
	ds_write_b128 v4, v[12:15]
	v_mul_lo_u32 v4, v81, s15
	v_add_u32_e32 v4, 0, v4
	v_and_b32_e32 v5, 16, v81
	v_add3_u32 v4, v4, v5, v2
	ds_write_b128 v4, v[20:23]
	v_mul_lo_u32 v4, v104, s15
	v_add_u32_e32 v4, 0, v4
	v_and_b32_e32 v5, 16, v104
	v_add3_u32 v4, v4, v5, v2
	ds_write_b128 v4, v[24:27]
	v_mul_lo_u32 v4, v105, s15
	v_add_u32_e32 v4, 0, v4
	v_and_b32_e32 v5, 16, v105
	v_add3_u32 v4, v4, v5, v2
	ds_write_b128 v4, v[28:31]
	v_mul_lo_u32 v4, v106, s15
	v_add_u32_e32 v4, 0, v4
	v_and_b32_e32 v5, 16, v106
	v_add3_u32 v4, v4, v5, v2
	ds_write_b128 v4, v[36:39]
	v_mul_lo_u32 v4, v107, s15
	v_add_u32_e32 v4, 0, v4
	v_and_b32_e32 v5, 16, v107
	s_movk_i32 s2, 0x420
	v_add3_u32 v2, v4, v5, v2
	v_mul_lo_u32 v4, v3, s2
	s_add_i32 s36, 0, 0x12000
	s_waitcnt vmcnt(8)
	ds_write_b128 v2, v[40:43]
	v_and_b32_e32 v2, 0x3f0, v48
	v_add_u32_e32 v4, s36, v4
	v_and_b32_e32 v3, 16, v3
	v_add3_u32 v3, v4, v3, v2
	s_waitcnt vmcnt(7)
	ds_write_b128 v3, v[44:47]
	v_mul_lo_u32 v3, v49, s2
	v_add_u32_e32 v3, s36, v3
	v_and_b32_e32 v4, 16, v49
	v_add3_u32 v3, v3, v4, v2
	s_waitcnt vmcnt(6)
	ds_write_b128 v3, v[72:75]
	v_mul_lo_u32 v3, v67, s2
	v_add_u32_e32 v3, s36, v3
	v_and_b32_e32 v4, 16, v67
	v_add3_u32 v3, v3, v4, v2
	s_waitcnt vmcnt(5)
	ds_write_b128 v3, v[76:79]
	v_mul_lo_u32 v3, v80, s2
	v_add_u32_e32 v3, s36, v3
	v_and_b32_e32 v4, 16, v80
	v_add3_u32 v3, v3, v4, v2
	s_waitcnt vmcnt(4)
	ds_write_b128 v3, v[84:87]
	v_mul_lo_u32 v3, v108, s2
	v_add_u32_e32 v3, s36, v3
	v_and_b32_e32 v4, 16, v108
	v_add3_u32 v3, v3, v4, v2
	s_waitcnt vmcnt(3)
	ds_write_b128 v3, v[88:91]
	v_mul_lo_u32 v3, v109, s2
	v_add_u32_e32 v3, s36, v3
	v_and_b32_e32 v4, 16, v109
	v_add3_u32 v3, v3, v4, v2
	s_waitcnt vmcnt(2)
	ds_write_b128 v3, v[92:95]
	v_mul_lo_u32 v3, v110, s2
	v_add_u32_e32 v3, s36, v3
	v_and_b32_e32 v4, 16, v110
	s_cmp_gt_i32 s73, -1
	v_add3_u32 v3, v3, v4, v2
	s_cselect_b64 s[44:45], -1, 0
	s_waitcnt vmcnt(1)
	ds_write_b128 v3, v[96:99]
	v_mul_lo_u32 v3, v111, s2
	s_and_b64 s[2:3], s[44:45], exec
	s_cselect_b32 s4, s73, 0
	s_lshr_b32 s3, s4, 13
	s_lshr_b32 s2, s4, 8
	s_lshl_b32 s5, s3, 5
	s_sub_i32 s2, s2, s5
	s_cmp_eq_u32 s3, 1
	s_cselect_b32 s3, s63, s65
	s_cselect_b32 s5, s62, s64
	s_cmpk_lt_u32 s4, 0x2000
	s_cselect_b32 s3, s61, s3
	s_cselect_b32 s5, s60, s5
	s_add_u32 s6, s3, s70
	s_addc_u32 s5, s5, 0
	s_ashr_i32 s3, s2, 31
	s_lshl_b64 s[2:3], s[2:3], 22
	s_add_u32 s2, s6, s2
	s_addc_u32 s3, s5, s3
	s_lshl_b32 s5, s4, 2
	s_and_b32 s5, s5, 0x3c0
	v_readlane_b32 s6, v239, 17
	s_or_b32 s5, s5, s6
	s_lshl_b32 s5, s5, 12
	s_add_u32 s2, s2, s5
	s_addc_u32 s3, s3, 0
	s_lshl_b32 s4, s4, 8
	v_add_u32_e32 v3, s36, v3
	v_and_b32_e32 v4, 16, v111
	s_and_b32 s4, s4, 0xf00
	v_and_b32_e32 v1, 63, v34
	v_add3_u32 v2, v3, v4, v2
	s_add_u32 s2, s2, s4
	s_waitcnt vmcnt(0)
	ds_write_b128 v2, v[100:103]
	s_waitcnt lgkmcnt(0)
	s_barrier
	s_addc_u32 s3, s3, 0
	v_lshlrev_b32_e32 v2, 3, v1
	v_mov_b32_e32 v3, v167
	v_lshl_add_u64 v[4:5], s[2:3], 0, v[2:3]
	global_load_dwordx2 v[84:85], v2, s[2:3] nt
	s_movk_i32 s2, 0x2000
	v_add_co_u32_e32 v2, vcc, s2, v4
	s_movk_i32 s2, 0x6000
	s_nop 0
	v_addc_co_u32_e32 v3, vcc, 0, v5, vcc
	global_load_dwordx2 v[90:91], v[2:3], off offset:-4096 nt
	global_load_dwordx2 v[86:87], v[2:3], off nt
	v_add_co_u32_e32 v2, vcc, s77, v4
	v_readlane_b32 s7, v239, 18
	s_nop 0
	v_addc_co_u32_e32 v3, vcc, 0, v5, vcc
	global_load_dwordx2 v[96:97], v[2:3], off offset:-4096 nt
	global_load_dwordx2 v[88:89], v[2:3], off nt
	v_add_co_u32_e32 v2, vcc, s2, v4
	s_mov_b32 s2, 0xa000
	s_nop 0
	v_addc_co_u32_e32 v3, vcc, 0, v5, vcc
	global_load_dwordx2 v[106:107], v[2:3], off offset:-4096 nt
	global_load_dwordx2 v[100:101], v[2:3], off nt
	v_add_co_u32_e32 v2, vcc, s82, v4
	v_and_b32_e32 v69, 3, v34
	s_nop 0
	v_addc_co_u32_e32 v3, vcc, 0, v5, vcc
	global_load_dwordx2 v[102:103], v[2:3], off offset:-4096 nt
	global_load_dwordx2 v[92:93], v[2:3], off nt
	v_add_co_u32_e32 v2, vcc, s2, v4
	s_mov_b32 s2, 0xc000
	s_nop 0
	v_addc_co_u32_e32 v3, vcc, 0, v5, vcc
	global_load_dwordx2 v[118:119], v[2:3], off offset:-4096 nt
	global_load_dwordx2 v[108:109], v[2:3], off nt
	v_add_co_u32_e32 v2, vcc, s2, v4
	s_mov_b32 s2, 0xe000
	s_nop 0
	v_addc_co_u32_e32 v3, vcc, 0, v5, vcc
	global_load_dwordx2 v[110:111], v[2:3], off offset:-4096 nt
	global_load_dwordx2 v[94:95], v[2:3], off nt
	v_add_co_u32_e32 v2, vcc, s2, v4
	s_mov_b32 s2, 0x10000
	s_nop 0
	v_addc_co_u32_e32 v3, vcc, 0, v5, vcc
	global_load_dwordx2 v[126:127], v[2:3], off offset:-4096 nt
	global_load_dwordx2 v[112:113], v[2:3], off nt
	v_add_co_u32_e32 v2, vcc, s2, v4
	s_mov_b32 s2, 0x12000
	s_nop 0
	v_addc_co_u32_e32 v3, vcc, 0, v5, vcc
	global_load_dwordx2 v[120:121], v[2:3], off offset:-4096 nt
	global_load_dwordx2 v[98:99], v[2:3], off nt
	v_add_co_u32_e32 v2, vcc, s2, v4
	s_mov_b32 s2, 0x14000
	s_nop 0
	v_addc_co_u32_e32 v3, vcc, 0, v5, vcc
	global_load_dwordx2 v[128:129], v[2:3], off offset:-4096 nt
	global_load_dwordx2 v[114:115], v[2:3], off nt
	v_add_co_u32_e32 v2, vcc, s2, v4
	s_mov_b32 s2, 0x16000
	s_nop 0
	v_addc_co_u32_e32 v3, vcc, 0, v5, vcc
	global_load_dwordx2 v[122:123], v[2:3], off offset:-4096 nt
	global_load_dwordx2 v[104:105], v[2:3], off nt
	v_add_co_u32_e32 v2, vcc, s2, v4
	s_mov_b32 s2, 0x18000
	s_nop 0
	v_addc_co_u32_e32 v3, vcc, 0, v5, vcc
	global_load_dwordx2 v[134:135], v[2:3], off offset:-4096 nt
	global_load_dwordx2 v[130:131], v[2:3], off nt
	v_add_co_u32_e32 v2, vcc, s2, v4
	s_mov_b32 s2, 0x1a000
	s_nop 0
	v_addc_co_u32_e32 v3, vcc, 0, v5, vcc
	global_load_dwordx2 v[132:133], v[2:3], off offset:-4096 nt
	global_load_dwordx2 v[116:117], v[2:3], off nt
	v_add_co_u32_e32 v2, vcc, s2, v4
	s_mov_b32 s2, 0x1c000
	s_nop 0
	v_addc_co_u32_e32 v3, vcc, 0, v5, vcc
	global_load_dwordx2 v[142:143], v[2:3], off offset:-4096 nt
	global_load_dwordx2 v[136:137], v[2:3], off nt
	v_add_co_u32_e32 v2, vcc, s2, v4
	s_mov_b32 s2, 0x1e000
	s_nop 0
	v_addc_co_u32_e32 v3, vcc, 0, v5, vcc
	global_load_dwordx2 v[138:139], v[2:3], off offset:-4096 nt
	global_load_dwordx2 v[124:125], v[2:3], off nt
	v_add_co_u32_e32 v2, vcc, s2, v4
	s_mov_b32 s2, 0x1f000
	s_nop 0
	v_addc_co_u32_e32 v3, vcc, 0, v5, vcc
	global_load_dwordx2 v[144:145], v[2:3], off offset:-4096 nt
	global_load_dwordx2 v[140:141], v[2:3], off nt
	v_add_co_u32_e32 v2, vcc, s2, v4
	v_or3_b32 v18, v68, v69, v70
	s_nop 0
	v_addc_co_u32_e32 v3, vcc, 0, v5, vcc
	global_load_dwordx2 v[146:147], v[2:3], off nt
	v_or_b32_e32 v3, 1, v166
	v_cmp_lt_u32_e64 s[4:5], v3, v19
	v_or_b32_e32 v3, 2, v166
	v_cmp_lt_u32_e64 s[6:7], v3, v19
	v_or_b32_e32 v3, 3, v166
	v_cmp_lt_u32_e64 s[8:9], v3, v19
	v_or_b32_e32 v3, 4, v166
	v_cmp_lt_u32_e64 s[10:11], v3, v19
	v_or_b32_e32 v3, 5, v166
	v_readlane_b32 s14, v239, 15
	v_cmp_lt_u32_e64 s[12:13], v3, v19
	v_add_u32_e32 v2, 0, v70
	v_or_b32_e32 v3, s14, v18
	v_mul_lo_u32 v3, v3, s15
	v_add3_u32 v28, v2, v166, v3
	ds_read_b128 v[2:5], v28
	ds_read_b128 v[20:23], v28 offset:32
	v_or_b32_e32 v6, 6, v166
	v_cmp_lt_u32_e64 s[14:15], v6, v19
	v_or_b32_e32 v6, 7, v166
	v_cmp_lt_u32_e64 s[16:17], v6, v19
	v_or_b32_e32 v6, 8, v166
	v_cmp_lt_u32_e64 s[18:19], v6, v19
	s_waitcnt lgkmcnt(1)
	v_mfma_f32_32x32x16_bf16 v[2:17], v[2:5], v[50:53], 0
	v_or_b32_e32 v24, 9, v166
	v_cmp_lt_u32_e64 s[20:21], v24, v19
	v_or_b32_e32 v24, 10, v166
	v_cmp_lt_u32_e64 s[22:23], v24, v19
	v_or_b32_e32 v24, 11, v166
	v_cmp_lt_u32_e64 s[24:25], v24, v19
	ds_read_b128 v[24:27], v28 offset:64
	s_waitcnt lgkmcnt(1)
	v_mfma_f32_32x32x16_bf16 v[2:17], v[20:23], v[54:57], v[2:17]
	v_or_b32_e32 v20, 13, v166
	v_cmp_lt_u32_e64 s[28:29], v20, v19
	v_or_b32_e32 v20, 14, v166
	v_cmp_lt_u32_e64 s[30:31], v20, v19
	ds_read_b128 v[20:23], v28 offset:96
	v_or_b32_e32 v29, 12, v166
	v_cmp_lt_u32_e64 s[26:27], v29, v19
	s_waitcnt lgkmcnt(1)
	v_mfma_f32_32x32x16_bf16 v[2:17], v[24:27], v[58:61], v[2:17]
	v_and_b32_e32 v25, 64, v192
	v_xor_b32_e32 v24, 32, v192
	v_add_u32_e32 v25, 64, v25
	v_cmp_lt_i32_e32 vcc, v24, v25
	v_or_b32_e32 v29, 15, v166
	v_cmp_lt_u32_e64 s[34:35], v29, v19
	v_cndmask_b32_e32 v24, v192, v24, vcc
	s_waitcnt lgkmcnt(0)
	v_mfma_f32_32x32x16_bf16 v[2:17], v[20:23], v[62:65], v[2:17]
	v_lshlrev_b32_e32 v156, 2, v24
	v_cmp_lt_u32_e64 s[2:3], v166, v19
	v_and_b32_e32 v66, 32, v34
	v_mul_u32_u24_e32 v35, 0x420, v18
	s_mov_b64 s[50:51], -1
	s_nop 6
	v_pk_mul_f32 v[2:3], v[2:3], s[88:89] op_sel_hi:[1,0]
	s_nop 0
	v_min_f32_e32 v2, 0x42700000, v2
	v_pk_mul_f32 v[4:5], v[4:5], s[88:89] op_sel_hi:[1,0]
	v_exp_f32_e32 v22, v2
	v_min_f32_e32 v2, 0x42700000, v3
	v_exp_f32_e32 v23, v2
	v_min_f32_e32 v2, 0x42700000, v4
	v_pk_mul_f32 v[6:7], v[6:7], s[88:89] op_sel_hi:[1,0]
	v_exp_f32_e32 v24, v2
	v_min_f32_e32 v2, 0x42700000, v5
	v_exp_f32_e32 v25, v2
	v_min_f32_e32 v2, 0x42700000, v6
	v_pk_mul_f32 v[8:9], v[8:9], s[88:89] op_sel_hi:[1,0]
	v_exp_f32_e32 v6, v2
	v_min_f32_e32 v2, 0x42700000, v7
	v_exp_f32_e32 v7, v2
	v_min_f32_e32 v2, 0x42700000, v8
	v_pk_mul_f32 v[10:11], v[10:11], s[88:89] op_sel_hi:[1,0]
	v_exp_f32_e32 v8, v2
	v_min_f32_e32 v2, 0x42700000, v9
	v_exp_f32_e32 v9, v2
	v_min_f32_e32 v2, 0x42700000, v10
	v_pk_mul_f32 v[12:13], v[12:13], s[88:89] op_sel_hi:[1,0]
	v_exp_f32_e32 v10, v2
	v_min_f32_e32 v2, 0x42700000, v11
	v_exp_f32_e32 v11, v2
	v_min_f32_e32 v2, 0x42700000, v12
	v_pk_mul_f32 v[14:15], v[14:15], s[88:89] op_sel_hi:[1,0]
	v_exp_f32_e32 v12, v2
	v_min_f32_e32 v2, 0x42700000, v13
	v_exp_f32_e32 v13, v2
	v_min_f32_e32 v2, 0x42700000, v14
	v_pk_mul_f32 v[16:17], v[16:17], s[88:89] op_sel_hi:[1,0]
	v_exp_f32_e32 v26, v2
	v_min_f32_e32 v2, 0x42700000, v15
	v_min_f32_e32 v3, 0x42700000, v17
	v_exp_f32_e32 v27, v2
	v_min_f32_e32 v2, 0x42700000, v16
	v_exp_f32_e32 v14, v3
	v_exp_f32_e32 v40, v2
	v_add_f32_e32 v32, 1.0, v27
	v_add_f32_e32 v31, 1.0, v26
	v_add_f32_e32 v2, 1.0, v14
	v_add_f32_e32 v33, 1.0, v40
	v_rcp_f32_e32 v2, v2
	v_rcp_f32_e32 v33, v33
	v_rcp_f32_e32 v32, v32
	v_add_f32_e32 v30, 1.0, v13
	v_rcp_f32_e32 v31, v31
	v_add_f32_e32 v29, 1.0, v12
	v_rcp_f32_e32 v30, v30
	v_cndmask_b32_e64 v15, 1.0, v2, s[34:35]
	v_add_f32_e32 v28, 1.0, v11
	v_rcp_f32_e32 v29, v29
	v_cndmask_b32_e64 v33, 1.0, v33, s[30:31]
	v_add_f32_e32 v3, 1.0, v22
	v_add_f32_e32 v4, 1.0, v23
	v_add_f32_e32 v5, 1.0, v24
	v_add_f32_e32 v21, 1.0, v10
	v_rcp_f32_e32 v28, v28
	v_cndmask_b32_e64 v32, 1.0, v32, s[28:29]
	v_mul_f32_e32 v41, v33, v15
	v_rcp_f32_e32 v3, v3
	v_rcp_f32_e32 v4, v4
	v_rcp_f32_e32 v5, v5
	v_add_f32_e32 v20, 1.0, v9
	v_rcp_f32_e32 v21, v21
	v_cndmask_b32_e64 v31, 1.0, v31, s[26:27]
	v_mul_f32_e32 v32, v32, v41
	v_add_f32_e32 v19, 1.0, v8
	v_rcp_f32_e32 v20, v20
	v_cndmask_b32_e64 v30, 1.0, v30, s[24:25]
	v_mul_f32_e32 v31, v31, v32
	v_add_f32_e32 v17, 1.0, v7
	v_rcp_f32_e32 v19, v19
	v_cndmask_b32_e64 v29, 1.0, v29, s[22:23]
	v_mul_f32_e32 v30, v30, v31
	v_add_f32_e32 v16, 1.0, v6
	v_rcp_f32_e32 v17, v17
	v_cndmask_b32_e64 v28, 1.0, v28, s[20:21]
	v_mul_f32_e32 v29, v29, v30
	v_cndmask_b32_e64 v2, 1.0, v3, s[2:3]
	v_cndmask_b32_e64 v3, 1.0, v4, s[4:5]
	v_cndmask_b32_e64 v4, 1.0, v5, s[6:7]
	v_add_f32_e32 v5, 1.0, v25
	v_rcp_f32_e32 v16, v16
	v_cndmask_b32_e64 v21, 1.0, v21, s[18:19]
	v_mul_f32_e32 v28, v28, v29
	v_rcp_f32_e32 v5, v5
	v_cndmask_b32_e64 v20, 1.0, v20, s[16:17]
	v_mul_f32_e32 v33, v21, v28
	v_cndmask_b32_e64 v19, 1.0, v19, s[14:15]
	v_mul_f32_e32 v42, v20, v33
	v_cndmask_b32_e64 v17, 1.0, v17, s[12:13]
	v_mul_f32_e32 v43, v19, v42
	v_cndmask_b32_e64 v16, 1.0, v16, s[10:11]
	v_mul_f32_e32 v17, v17, v43
	v_cndmask_b32_e64 v5, 1.0, v5, s[8:9]
	v_mul_f32_e32 v16, v16, v17
	v_mul_f32_e32 v44, v5, v16
	v_mul_f32_e32 v45, v4, v44
	v_mul_f32_e32 v46, v3, v45
	v_mul_f32_e32 v47, v2, v46
	ds_bpermute_b32 v48, v156, v47
	v_add3_u32 v2, s36, v70, v66
	v_readlane_b32 s36, v239, 16
	s_waitcnt lgkmcnt(0)
	v_mul_f32_e32 v157, v47, v48
	v_add3_u32 v49, v2, s36, v35
	v_cmp_gt_u32_e64 s[36:37], 32, v1
	ds_read_b128 v[2:5], v49
	ds_read_b128 v[36:39], v49 offset:16
	ds_read_b128 v[18:21], v49 offset:33792
	v_cndmask_b32_e64 v48, 1.0, v48, s[36:37]
	v_mul_f32_e32 v16, v48, v16
	v_mul_f32_e32 v6, v6, v16
	v_mul_f32_e32 v16, v48, v17
	v_mul_f32_e32 v15, v48, v15
	v_mul_f32_e32 v7, v7, v16
	v_mul_f32_e32 v16, v48, v43
	v_mul_f32_e32 v14, v14, v15
	v_mul_f32_e32 v8, v8, v16
	v_mul_f32_e32 v16, v48, v42
	v_cndmask_b32_e64 v67, 0, v14, s[34:35]
	v_mul_f32_e32 v14, v48, v47
	v_mul_f32_e32 v9, v9, v16
	v_mul_f32_e32 v16, v48, v33
	v_mul_f32_e32 v14, v22, v14
	v_mul_f32_e32 v22, v48, v45
	v_mul_f32_e32 v10, v10, v16
	v_mul_f32_e32 v15, v48, v46
	v_mul_f32_e32 v22, v24, v22
	v_cndmask_b32_e64 v42, 0, v10, s[18:19]
	v_mul_f32_e32 v10, v48, v28
	v_mul_f32_e32 v15, v23, v15
	v_cndmask_b32_e64 v23, 0, v22, s[6:7]
	v_mul_f32_e32 v22, v48, v44
	v_mul_f32_e32 v10, v11, v10
	v_mul_f32_e32 v22, v25, v22
	v_cndmask_b32_e64 v43, 0, v10, s[20:21]
	v_mul_f32_e32 v10, v48, v29
	v_cndmask_b32_e64 v14, 0, v14, s[2:3]
	v_cndmask_b32_e64 v15, 0, v15, s[4:5]
	v_cndmask_b32_e64 v24, 0, v22, s[8:9]
	v_cndmask_b32_e64 v6, 0, v6, s[10:11]
	v_cndmask_b32_e64 v7, 0, v7, s[12:13]
	v_cndmask_b32_e64 v8, 0, v8, s[14:15]
	v_cndmask_b32_e64 v9, 0, v9, s[16:17]
	v_mul_f32_e32 v10, v12, v10
	v_cndmask_b32_e64 v44, 0, v10, s[22:23]
	v_mul_f32_e32 v10, v48, v30
	v_cvt_pk_bf16_f32 v22, v14, v15
	v_cvt_pk_bf16_f32 v23, v23, v24
	v_cvt_pk_bf16_f32 v24, v6, v7
	v_cvt_pk_bf16_f32 v25, v8, v9
	v_mul_f32_e32 v28, v13, v10
	v_cndmask_b32_e64 v45, 0, v28, s[24:25]
	s_waitcnt lgkmcnt(2)
	v_mfma_f32_32x32x16_bf16 v[2:17], v[2:5], v[22:25], 0
	v_mul_f32_e32 v28, v48, v31
	v_mul_f32_e32 v26, v26, v28
	v_cndmask_b32_e64 v46, 0, v26, s[26:27]
	v_mul_f32_e32 v26, v48, v32
	v_mul_f32_e32 v41, v48, v41
	v_mul_f32_e32 v26, v27, v26
	v_mul_f32_e32 v40, v40, v41
	v_cndmask_b32_e64 v47, 0, v26, s[28:29]
	v_cndmask_b32_e64 v48, 0, v40, s[30:31]
	v_cvt_pk_bf16_f32 v40, v42, v43
	v_cvt_pk_bf16_f32 v41, v44, v45
	v_cvt_pk_bf16_f32 v42, v46, v47
	v_cvt_pk_bf16_f32 v43, v48, v67
	s_waitcnt lgkmcnt(0)
	v_mfma_f32_32x32x16_bf16 v[18:33], v[18:21], v[22:25], 0
	v_cmp_eq_f32_e32 vcc, 0, v157
	s_cmp_eq_u64 vcc, exec
	v_mfma_f32_32x32x16_bf16 v[2:17], v[36:39], v[40:43], v[2:17]
	ds_read_b128 v[36:39], v49 offset:33808
	s_waitcnt lgkmcnt(0)
	v_mfma_f32_32x32x16_bf16 v[18:33], v[36:39], v[40:43], v[18:33]
	s_cbranch_scc1 .LBB0_307
	s_cmp_eq_u32 s42, 0
	s_cbranch_scc1 .LBB0_308
	v_bfe_u32 v36, v34, 2, 1
	v_bfe_u32 v34, v34, 3, 2
	v_mul_u32_u24_e32 v36, 0x910, v36
	v_mul_u32_u24_e32 v34, 0x240, v34
	v_readlane_b32 s52, v239, 39
	s_sub_i32 s42, s42, 32
	s_nop 0
	v_add3_u32 v34, s52, v36, v34
	v_mul_u32_u24_e32 v36, 0x90, v69
	v_readlane_b32 s52, v239, 51
	v_add3_u32 v67, v34, v36, v166
	s_nop 0
	v_add_u32_e32 v34, s52, v35
	v_add3_u32 v71, v34, v66, v70
	ds_read_b128 v[200:203], v67
	ds_read_b128 v[204:207], v67 offset:32
	ds_read_b128 v[208:211], v67 offset:64
	ds_read_b128 v[212:215], v67 offset:96
	s_branch .LBB0_305

.LBB0_305:
	v_add_u32_e32 v173, 0, v71
	v_add_u32_e32 v172, 0x121c0, v173
	v_add_u32_e32 v175, 0x121d0, v173
	s_waitcnt lgkmcnt(3)
	v_mfma_f32_32x32x16_bf16 v[34:49], v[200:203], v[50:53], 0
	s_mov_b64 s[54:55], -1
	s_waitcnt lgkmcnt(2)
	v_mfma_f32_32x32x16_bf16 v[34:49], v[204:207], v[54:57], v[34:49]
	s_waitcnt lgkmcnt(1)
	v_mfma_f32_32x32x16_bf16 v[34:49], v[208:211], v[58:61], v[34:49]
	s_waitcnt lgkmcnt(0)
	v_mfma_f32_32x32x16_bf16 v[34:49], v[212:215], v[62:65], v[34:49]
	v_add_u32_e32 v76, 0xffffee00, v67
	v_max_i32_e32 v76, 0, v76
	ds_read_b128 v[200:203], v76
	ds_read_b128 v[204:207], v76 offset:32
	ds_read_b128 v[208:211], v76 offset:64
	ds_read_b128 v[212:215], v76 offset:96
	s_nop 5
	v_pk_mul_f32 v[46:47], v[46:47], s[88:89] op_sel_hi:[1,0]
	v_pk_mul_f32 v[48:49], v[48:49], s[88:89] op_sel_hi:[1,0]
	v_min_f32_e32 v47, 0x42700000, v47
	v_pk_mul_f32 v[44:45], v[44:45], s[88:89] op_sel_hi:[1,0]
	v_exp_f32_e32 v151, v47
	v_min_f32_e32 v47, 0x42700000, v48
	v_min_f32_e32 v44, 0x42700000, v44
	v_exp_f32_e32 v152, v47
	v_min_f32_e32 v47, 0x42700000, v49
	v_exp_f32_e32 v148, v44
	v_min_f32_e32 v44, 0x42700000, v45
	v_exp_f32_e32 v153, v47
	v_exp_f32_e32 v149, v44
	v_min_f32_e32 v44, 0x42700000, v46
	v_pk_mul_f32 v[42:43], v[42:43], s[88:89] op_sel_hi:[1,0]
	v_exp_f32_e32 v150, v44
	v_min_f32_e32 v42, 0x42700000, v42
	v_exp_f32_e32 v80, v42
	v_min_f32_e32 v42, 0x42700000, v43
	v_add_f32_e32 v48, 1.0, v152
	v_add_f32_e32 v49, 1.0, v153
	v_pk_mul_f32 v[40:41], v[40:41], s[88:89] op_sel_hi:[1,0]
	v_exp_f32_e32 v81, v42
	v_add_f32_e32 v47, 1.0, v151
	v_rcp_f32_e32 v48, v48
	v_rcp_f32_e32 v155, v49
	v_min_f32_e32 v41, 0x42700000, v41
	v_add_f32_e32 v46, 1.0, v150
	v_rcp_f32_e32 v47, v47
	v_pk_mul_f32 v[38:39], v[38:39], s[88:89] op_sel_hi:[1,0]
	v_min_f32_e32 v40, 0x42700000, v40
	v_exp_f32_e32 v79, v41
	v_add_f32_e32 v45, 1.0, v149
	v_rcp_f32_e32 v46, v46
	v_min_f32_e32 v39, 0x42700000, v39
	v_exp_f32_e32 v78, v40
	v_add_f32_e32 v44, 1.0, v148
	v_rcp_f32_e32 v45, v45
	v_pk_mul_f32 v[36:37], v[36:37], s[88:89] op_sel_hi:[1,0]
	v_min_f32_e32 v38, 0x42700000, v38
	v_exp_f32_e32 v77, v39
	v_add_f32_e32 v43, 1.0, v81
	v_rcp_f32_e32 v44, v44
	v_mul_f32_e32 v154, v48, v155
	v_min_f32_e32 v37, 0x42700000, v37
	v_exp_f32_e32 v76, v38
	v_add_f32_e32 v42, 1.0, v80
	v_rcp_f32_e32 v43, v43
	v_mul_f32_e32 v159, v47, v154
	v_pk_mul_f32 v[34:35], v[34:35], s[88:89] op_sel_hi:[1,0]
	v_min_f32_e32 v36, 0x42700000, v36
	v_exp_f32_e32 v75, v37
	v_add_f32_e32 v41, 1.0, v79
	v_rcp_f32_e32 v42, v42
	v_mul_f32_e32 v158, v46, v159
	v_min_f32_e32 v35, 0x42700000, v35
	v_exp_f32_e32 v74, v36
	v_add_f32_e32 v40, 1.0, v78
	v_rcp_f32_e32 v41, v41
	v_mul_f32_e32 v161, v45, v158
	v_min_f32_e32 v34, 0x42700000, v34
	v_exp_f32_e32 v73, v35
	v_add_f32_e32 v39, 1.0, v77
	v_rcp_f32_e32 v40, v40
	v_mul_f32_e32 v160, v44, v161
	v_exp_f32_e32 v72, v34
	v_add_f32_e32 v38, 1.0, v76
	v_rcp_f32_e32 v39, v39
	v_mul_f32_e32 v163, v43, v160
	v_add_f32_e32 v37, 1.0, v75
	v_rcp_f32_e32 v38, v38
	v_mul_f32_e32 v162, v42, v163
	v_add_f32_e32 v36, 1.0, v74
	v_rcp_f32_e32 v37, v37
	v_mul_f32_e32 v43, v41, v162
	v_add_f32_e32 v35, 1.0, v73
	v_rcp_f32_e32 v36, v36
	v_mul_f32_e32 v42, v40, v43
	v_add_f32_e32 v34, 1.0, v72
	v_rcp_f32_e32 v35, v35
	v_mul_f32_e32 v45, v39, v42
	v_rcp_f32_e32 v34, v34
	v_mul_f32_e32 v44, v38, v45
	v_mul_f32_e32 v47, v37, v44
	v_mul_f32_e32 v46, v36, v47
	v_mul_f32_e32 v165, v35, v46
	v_mul_f32_e32 v164, v34, v165
	ds_bpermute_b32 v174, v156, v164
	ds_read_b128 v[34:37], v172
	v_add_u32_e32 v38, 0x1a5c0, v173
	ds_read_b128 v[38:41], v38
	s_waitcnt lgkmcnt(2)
	v_cndmask_b32_e64 v48, 1.0, v174, s[36:37]
	v_mul_f32_e32 v172, v157, v48
	v_pk_mul_f32 v[48:49], v[172:173], v[164:165] op_sel_hi:[0,1]
	v_pk_mul_f32 v[46:47], v[172:173], v[46:47] op_sel_hi:[0,1]
	v_pk_mul_f32 v[44:45], v[172:173], v[44:45] op_sel_hi:[0,1]
	v_pk_mul_f32 v[42:43], v[172:173], v[42:43] op_sel_hi:[0,1]
	v_pk_mul_f32 v[48:49], v[72:73], v[48:49]
	v_pk_mul_f32 v[46:47], v[74:75], v[46:47]
	v_pk_mul_f32 v[44:45], v[76:77], v[44:45]
	v_pk_mul_f32 v[72:73], v[78:79], v[42:43]
	v_cvt_pk_bf16_f32 v42, v48, v49
	v_cvt_pk_bf16_f32 v43, v46, v47
	v_cvt_pk_bf16_f32 v44, v44, v45
	v_cvt_pk_bf16_f32 v45, v72, v73
	ds_read_b128 v[46:49], v175
	v_pk_mul_f32 v[76:77], v[172:173], v[158:159] op_sel_hi:[0,1]
	s_waitcnt lgkmcnt(2)
	v_mfma_f32_32x32x16_bf16 v[2:17], v[34:37], v[42:45], v[2:17]
	v_mul_f32_e64 v34, v172, v162
	v_mul_f32_e64 v35, v172, v163
	v_add_u32_e32 v36, 0x1a5d0, v173
	v_mul_f32_e64 v72, v80, v34
	v_mul_f32_e64 v73, v81, v35
	v_pk_mul_f32 v[34:35], v[172:173], v[160:161] op_sel_hi:[0,1]
	v_pk_mul_f32 v[74:75], v[148:149], v[34:35]
	ds_read_b128 v[34:37], v36
	s_waitcnt lgkmcnt(2)
	v_mfma_f32_32x32x16_bf16 v[18:33], v[38:41], v[42:45], v[18:33]
	v_mul_f32_e64 v38, v172, v154
	v_mul_f32_e64 v39, v172, v155
	v_mul_f32_e64 v40, v150, v76
	v_mul_f32_e64 v41, v151, v77
	v_mul_f32_e64 v42, v152, v38
	v_mul_f32_e64 v43, v153, v39
	v_cvt_pk_bf16_f32 v38, v72, v73
	v_cvt_pk_bf16_f32 v39, v74, v75
	v_cvt_pk_bf16_f32 v40, v40, v41
	v_cvt_pk_bf16_f32 v41, v42, v43
	v_mul_f32_e32 v42, v164, v174
	v_mul_f32_e32 v157, v157, v42
	s_waitcnt lgkmcnt(1)
	v_mfma_f32_32x32x16_bf16 v[2:17], v[46:49], v[38:41], v[2:17]
	v_cmp_eq_f32_e32 vcc, 0, v157
	s_cmp_eq_u64 vcc, exec
	s_waitcnt lgkmcnt(0)
	v_mfma_f32_32x32x16_bf16 v[18:33], v[34:37], v[38:41], v[18:33]
	s_cbranch_scc0 .LBB0_304
	s_mov_b64 s[52:53], -1
	s_branch .LBB0_309
